# baseline (speedup 1.0000x reference)
_Z9proj_gemmPKfS0_S0_PK14__hip_bfloat16S0_S0_S0_PS1_:
	s_bitcmp1_b32 s2, 3
	s_cbranch_scc0 .Lno_sleep
	s_sleep 20
.Lno_sleep:
	s_lshl_b32 s3, s2, 2
	s_load_dwordx8 s[8:15], s[0:1], 0x0
	s_and_b32 s3, s3, 28
	s_bfe_u32 s30, s2, 0x20005
	s_lshr_b32 s6, s2, 3
	s_ashr_i32 s18, s2, 7
	s_lshr_b32 s7, s2, 5
	s_or_b32 s20, s3, s30
	s_bfe_u32 s3, s2, 0x20003
	s_cmpk_lt_u32 s2, 0x80
	s_cselect_b64 s[16:17], -1, 0
	s_and_b64 s[4:5], s[16:17], exec
	s_waitcnt lgkmcnt(0)
	s_cselect_b32 s4, s9, s11
	s_cselect_b32 s5, s8, s10
	s_lshl_b32 s24, s20, 18
	s_lshl_b32 s8, s20, 20
	s_add_u32 s25, s5, s8
	s_addc_u32 s26, s4, 0
	s_ashr_i32 s19, s18, 31
	s_lshl_b64 s[4:5], s[18:19], 21
	s_add_u32 s4, s14, s4
	s_addc_u32 s5, s15, s5
	s_lshl_b32 s8, s3, 19
	s_add_u32 s27, s4, s8
	s_addc_u32 s28, s5, 0
	s_xor_b32 s6, s6, s18
	v_lshlrev_b32_e32 v1, 4, v0
	s_lshl_b32 s34, s6, 4
	v_lshlrev_b32_e32 v2, 3, v0
	v_and_b32_e32 v3, 0x1f0, v1
	s_movk_i32 s6, 0x200
	s_lshl_b32 s4, s20, 1
	s_mul_i32 s31, s18, 5
	s_xor_b32 s7, s7, s18
	v_lshrrev_b32_e32 v28, 6, v0
	s_and_b32 s35, s34, 16
	v_and_or_b32 v29, v2, s6, v3
	v_lshrrev_b32_e32 v2, 1, v0
	v_and_b32_e32 v3, 48, v1
	s_add_i32 s4, s4, s31
	v_bitop3_b32 v2, v2, v3, 32 bitop3:0x6c
	v_or_b32_e32 v30, s35, v28
	s_lshl_b32 s38, s7, 4
	s_and_b32 s5, s4, 15
	v_lshrrev_b32_e32 v2, 1, v2
	v_or_b32_e32 v32, 8, v30
	s_and_b32 s39, s38, 16
	v_and_or_b32 v178, v0, 32, v2
	v_lshlrev_b32_e32 v2, 3, v30
	v_lshrrev_b32_e32 v31, 6, v29
	s_movk_i32 s36, 0xb0
	v_lshlrev_b32_e32 v3, 3, v32
	s_movk_i32 s37, 0xf0
	v_or_b32_e32 v33, s39, v28
	s_lshl_b32 s33, s4, 6
	s_lshl_b32 s4, s5, 8
	v_and_or_b32 v2, v2, s36, v31
	v_and_or_b32 v12, v3, s37, v31
	v_lshlrev_b32_e32 v3, 3, v33
	v_or_b32_e32 v34, 8, v33
	s_add_u32 s20, s25, s4
	v_mov_b32_e32 v183, 0
	v_and_or_b32 v20, v3, s36, v31
	v_lshlrev_b32_e32 v3, 3, v34
	s_addc_u32 s21, s26, 0
	v_lshlrev_b32_e32 v180, 12, v2
	v_mov_b32_e32 v181, v183
	v_and_or_b32 v22, v3, s37, v31
	v_lshl_add_u64 v[2:3], s[20:21], 0, v[180:181]
	v_lshlrev_b32_e32 v182, 2, v178
	v_lshl_add_u64 v[10:11], v[2:3], 0, v[182:183]
	v_lshlrev_b32_e32 v184, 12, v12
	v_mov_b32_e32 v185, v183
	s_lshl_b32 s4, s5, 7
	global_load_dwordx4 v[2:5], v[10:11], off offset:16
	global_load_dwordx4 v[6:9], v[10:11], off
	v_lshl_add_u64 v[10:11], s[20:21], 0, v[184:185]
	s_add_u32 s22, s27, s4
	v_lshl_add_u64 v[14:15], v[10:11], 0, v[182:183]
	s_addc_u32 s23, s28, 0
	v_lshlrev_b32_e32 v186, 11, v20
	v_mov_b32_e32 v187, v183
	global_load_dwordx4 v[10:13], v[14:15], off offset:16
	global_load_dwordx4 v[16:19], v[14:15], off
	v_lshl_add_u64 v[20:21], s[22:23], 0, v[186:187]
	v_lshlrev_b32_e32 v14, 1, v178
	v_mov_b32_e32 v15, v183
	v_lshlrev_b32_e32 v188, 11, v22
	v_mov_b32_e32 v189, v183
	v_lshl_add_u64 v[24:25], v[20:21], 0, v[14:15]
	v_lshl_add_u64 v[20:21], s[22:23], 0, v[188:189]
	v_lshl_add_u64 v[26:27], v[20:21], 0, v[14:15]
	global_load_dwordx4 v[20:23], v[24:25], off
	global_load_dwordx4 v[50:53], v[26:27], off
	v_bfe_u32 v24, v0, 5, 1
	v_and_or_b32 v25, v30, 22, v24
	v_lshl_or_b32 v208, v25, 10, v29
	v_and_or_b32 v25, v32, 30, v24
	v_lshl_or_b32 v205, v25, 10, v29
	v_bitop3_b32 v25, s34, 16, v28 bitop3:0x26
	v_and_or_b32 v26, v25, 22, v24
	v_lshl_or_b32 v204, v26, 10, v29
	v_bitop3_b32 v26, s35, v28, 24 bitop3:0xde
	v_and_or_b32 v27, v26, 30, v24
	v_lshl_or_b32 v201, v27, 10, v29
	v_and_or_b32 v27, v33, 22, v24
	v_lshl_or_b32 v206, v27, 10, v29
	v_and_or_b32 v27, v34, 30, v24
	s_load_dwordx8 s[4:11], s[0:1], 0x20
	v_lshl_or_b32 v207, v27, 10, v29
	v_bitop3_b32 v27, s38, 16, v28 bitop3:0x26
	v_bitop3_b32 v28, s39, v28, 24 bitop3:0xde
	v_and_or_b32 v30, v27, 22, v24
	v_and_or_b32 v24, v28, 30, v24
	v_and_b32_e32 v179, 15, v0
	v_lshl_or_b32 v202, v30, 10, v29
	v_lshl_or_b32 v203, v24, 10, v29
	v_lshlrev_b32_e32 v24, 3, v28
	v_lshlrev_b32_e32 v29, 2, v0
	v_lshrrev_b32_e32 v198, 8, v0
	v_lshlrev_b32_e32 v25, 3, v25
	v_lshlrev_b32_e32 v26, 3, v26
	v_lshlrev_b32_e32 v27, 3, v27
	v_and_or_b32 v28, v24, s37, v31
	v_and_b32_e32 v24, 48, v0
	v_and_b32_e32 v29, 32, v29
	v_lshlrev_b32_e32 v30, 6, v179
	s_mov_b32 s29, 0
	v_and_b32_e32 v199, 63, v0
	v_and_or_b32 v25, v25, s36, v31
	v_and_or_b32 v26, v26, s37, v31
	v_bfe_u32 v200, v0, 6, 2
	v_and_or_b32 v27, v27, s36, v31
	v_lshlrev_b32_e32 v80, 14, v198
	v_bitop3_b32 v81, v30, v29, v24 bitop3:0x36
	v_lshlrev_b32_e32 v190, 12, v25
	v_mov_b32_e32 v191, v183
	v_lshl_add_u64 v[24:25], s[20:21], 0, v[190:191]
	v_lshl_add_u64 v[24:25], v[24:25], 0, v[182:183]
	v_lshlrev_b32_e32 v192, 12, v26
	v_mov_b32_e32 v193, v183
	global_load_dwordx4 v[54:57], v[24:25], off offset:16
	global_load_dwordx4 v[58:61], v[24:25], off
	v_lshl_add_u64 v[24:25], s[20:21], 0, v[192:193]
	v_lshl_add_u64 v[24:25], v[24:25], 0, v[182:183]
	v_lshlrev_b32_e32 v194, 11, v27
	v_mov_b32_e32 v195, v183
	global_load_dwordx4 v[62:65], v[24:25], off offset:16
	global_load_dwordx4 v[66:69], v[24:25], off
	v_lshl_add_u64 v[24:25], s[22:23], 0, v[194:195]
	v_lshlrev_b32_e32 v196, 11, v28
	v_mov_b32_e32 v197, v183
	v_lshl_add_u64 v[24:25], v[24:25], 0, v[14:15]
	v_lshl_add_u64 v[26:27], s[22:23], 0, v[196:197]
	v_lshl_add_u64 v[26:27], v[26:27], 0, v[14:15]
	global_load_dwordx4 v[70:73], v[24:25], off
	global_load_dwordx4 v[74:77], v[26:27], off
	s_add_i32 s33, s33, 64
	s_and_b32 s20, s33, 0x3c0
	s_lshl_b32 s0, s20, 2
	s_add_u32 s0, s25, s0
	s_addc_u32 s1, s26, 0
	v_lshl_add_u64 v[24:25], s[0:1], 0, v[180:181]
	v_lshl_add_u64 v[24:25], v[24:25], 0, v[182:183]
	s_lshl_b32 s20, s20, 1
	global_load_dwordx4 v[42:45], v[24:25], off offset:16
	global_load_dwordx4 v[46:49], v[24:25], off
	v_lshl_add_u64 v[24:25], s[0:1], 0, v[184:185]
	s_add_u32 s20, s27, s20
	v_lshl_add_u64 v[24:25], v[24:25], 0, v[182:183]
	s_addc_u32 s21, s28, 0
	global_load_dwordx4 v[34:37], v[24:25], off offset:16
	global_load_dwordx4 v[38:41], v[24:25], off
	v_lshl_add_u64 v[24:25], s[20:21], 0, v[186:187]
	v_lshl_add_u64 v[24:25], v[24:25], 0, v[14:15]
	v_lshl_add_u64 v[26:27], s[20:21], 0, v[188:189]
	v_lshl_add_u64 v[78:79], v[26:27], 0, v[14:15]
	global_load_dwordx4 v[30:33], v[24:25], off
	global_load_dwordx4 v[26:29], v[78:79], off
	s_waitcnt vmcnt(16)
	v_cvt_pk_bf16_f32 v6, v6, v7
	v_cvt_pk_bf16_f32 v7, v8, v9
	v_cvt_pk_bf16_f32 v8, v2, v3
	v_add_u32_e32 v2, 0, v208
	v_cvt_pk_bf16_f32 v9, v4, v5
	ds_write_b128 v2, v[6:9]
	s_waitcnt vmcnt(14)
	v_cvt_pk_bf16_f32 v2, v16, v17
	v_add_u32_e32 v6, 0, v205
	v_cvt_pk_bf16_f32 v3, v18, v19
	v_cvt_pk_bf16_f32 v4, v10, v11
	v_cvt_pk_bf16_f32 v5, v12, v13
	ds_write_b128 v6, v[2:5]
	v_add_u32_e32 v2, 0, v206
	s_waitcnt vmcnt(13)
	ds_write_b128 v2, v[20:23] offset:32768
	v_add_u32_e32 v2, 0, v207
	s_waitcnt vmcnt(12)
	ds_write_b128 v2, v[50:53] offset:32768
	s_waitcnt vmcnt(10)
	v_cvt_pk_bf16_f32 v2, v58, v59
	v_add_u32_e32 v6, 0, v204
	v_cvt_pk_bf16_f32 v3, v60, v61
	v_cvt_pk_bf16_f32 v4, v54, v55
	v_cvt_pk_bf16_f32 v5, v56, v57
	ds_write_b128 v6, v[2:5]
	s_waitcnt vmcnt(8)
	v_cvt_pk_bf16_f32 v2, v66, v67
	v_add_u32_e32 v6, 0, v201
	v_cvt_pk_bf16_f32 v3, v68, v69
	v_cvt_pk_bf16_f32 v4, v62, v63
	v_cvt_pk_bf16_f32 v5, v64, v65
	ds_write_b128 v6, v[2:5]
	v_add_u32_e32 v2, 0, v202
	s_waitcnt vmcnt(7)
	ds_write_b128 v2, v[70:73] offset:32768
	v_add_u32_e32 v2, 0, v203
	s_waitcnt vmcnt(6)
	ds_write_b128 v2, v[74:77] offset:32768
	v_lshl_add_u64 v[2:3], s[0:1], 0, v[190:191]
	v_lshl_add_u64 v[2:3], v[2:3], 0, v[182:183]
	global_load_dwordx4 v[6:9], v[2:3], off offset:16
	global_load_dwordx4 v[22:25], v[2:3], off
	v_lshl_add_u64 v[2:3], s[0:1], 0, v[192:193]
	v_lshl_add_u64 v[16:17], v[2:3], 0, v[182:183]
	global_load_dwordx4 v[2:5], v[16:17], off offset:16
	global_load_dwordx4 v[10:13], v[16:17], off
	v_lshl_add_u64 v[16:17], s[20:21], 0, v[194:195]
	v_lshl_add_u64 v[50:51], v[16:17], 0, v[14:15]
	v_lshl_add_u64 v[16:17], s[20:21], 0, v[196:197]
	v_lshl_add_u64 v[52:53], v[16:17], 0, v[14:15]
	global_load_dwordx4 v[18:21], v[50:51], off
	global_load_dwordx4 v[14:17], v[52:53], off
	v_lshlrev_b32_e32 v50, 13, v200
	s_cmp_lg_u32 0, -1
	s_cselect_b32 s0, 0, 0
	v_add3_u32 v209, v80, s0, v81
	s_add_i32 s0, s0, 0x8000
	v_add3_u32 v210, v50, s0, v81
	s_lshl_b32 s0, s30, 1
	s_add_i32 s31, s31, s0
	s_lshl_b32 s0, s2, 3
	s_add_i32 s0, s0, s31
	s_waitcnt lgkmcnt(0)
	s_and_b32 s0, s0, 15
	s_lshl_b32 s0, s0, 6
	s_add_i32 s22, s0, 0x80
	v_mov_b32_e32 v50, v183
	v_mov_b32_e32 v51, v183
	v_mov_b32_e32 v52, v183
	v_mov_b32_e32 v53, v183
	v_mov_b32_e32 v54, v183
	v_mov_b32_e32 v55, v183
	v_mov_b32_e32 v56, v183
	v_mov_b32_e32 v57, v183
	v_mov_b32_e32 v58, v183
	v_mov_b32_e32 v59, v183
	v_mov_b32_e32 v60, v183
	v_mov_b32_e32 v61, v183
	v_mov_b32_e32 v62, v183
	v_mov_b32_e32 v63, v183
	v_mov_b32_e32 v64, v183
	v_mov_b32_e32 v65, v183
	v_mov_b32_e32 v66, v183
	v_mov_b32_e32 v67, v183
	v_mov_b32_e32 v68, v183
	v_mov_b32_e32 v69, v183
	v_mov_b32_e32 v70, v183
	v_mov_b32_e32 v71, v183
	v_mov_b32_e32 v72, v183
	v_mov_b32_e32 v73, v183
	v_mov_b32_e32 v74, v183
	v_mov_b32_e32 v75, v183
	v_mov_b32_e32 v76, v183
	v_mov_b32_e32 v77, v183
	v_mov_b32_e32 v78, v183
	v_mov_b32_e32 v79, v183
	v_mov_b32_e32 v80, v183
	v_mov_b32_e32 v81, v183
	v_mov_b32_e32 v82, v183
	v_mov_b32_e32 v83, v183
	v_mov_b32_e32 v84, v183
	v_mov_b32_e32 v85, v183
	v_mov_b32_e32 v86, v183
	v_mov_b32_e32 v87, v183
	v_mov_b32_e32 v88, v183
	v_mov_b32_e32 v89, v183
	v_mov_b32_e32 v90, v183
	v_mov_b32_e32 v91, v183
	v_mov_b32_e32 v92, v183
	v_mov_b32_e32 v93, v183
	v_mov_b32_e32 v94, v183
	v_mov_b32_e32 v95, v183
	v_mov_b32_e32 v96, v183
	v_mov_b32_e32 v97, v183
	v_mov_b32_e32 v98, v183
	v_mov_b32_e32 v99, v183
	v_mov_b32_e32 v100, v183
	v_mov_b32_e32 v101, v183
	v_mov_b32_e32 v102, v183
	v_mov_b32_e32 v103, v183
	v_mov_b32_e32 v104, v183
	v_mov_b32_e32 v105, v183
	v_mov_b32_e32 v106, v183
	v_mov_b32_e32 v107, v183
	v_mov_b32_e32 v108, v183
	v_mov_b32_e32 v109, v183
	v_mov_b32_e32 v110, v183
	v_mov_b32_e32 v111, v183
	v_mov_b32_e32 v112, v183
	v_mov_b32_e32 v113, v183
	v_mov_b32_e32 v114, v183
	v_mov_b32_e32 v115, v183
	v_mov_b32_e32 v116, v183
	v_mov_b32_e32 v117, v183
	v_mov_b32_e32 v118, v183
	v_mov_b32_e32 v119, v183
	v_mov_b32_e32 v120, v183
	v_mov_b32_e32 v121, v183
	v_mov_b32_e32 v122, v183
	v_mov_b32_e32 v123, v183
	v_mov_b32_e32 v124, v183
	v_mov_b32_e32 v125, v183
	v_mov_b32_e32 v126, v183
	v_mov_b32_e32 v127, v183
	v_mov_b32_e32 v128, v183
	v_mov_b32_e32 v129, v183
	v_mov_b32_e32 v130, v183
	v_mov_b32_e32 v131, v183
	v_mov_b32_e32 v132, v183
	v_mov_b32_e32 v133, v183
	v_mov_b32_e32 v134, v183
	v_mov_b32_e32 v135, v183
	v_mov_b32_e32 v136, v183
	v_mov_b32_e32 v137, v183
	v_mov_b32_e32 v138, v183
	v_mov_b32_e32 v139, v183
	v_mov_b32_e32 v140, v183
	v_mov_b32_e32 v141, v183
	v_mov_b32_e32 v142, v183
	v_mov_b32_e32 v143, v183
	v_mov_b32_e32 v144, v183
	v_mov_b32_e32 v145, v183
	v_mov_b32_e32 v146, v183
	v_mov_b32_e32 v147, v183
	v_mov_b32_e32 v148, v183
	v_mov_b32_e32 v149, v183
	v_mov_b32_e32 v150, v183
	v_mov_b32_e32 v151, v183
	v_mov_b32_e32 v152, v183
	v_mov_b32_e32 v153, v183
	v_mov_b32_e32 v154, v183
	v_mov_b32_e32 v155, v183
	v_mov_b32_e32 v156, v183
	v_mov_b32_e32 v157, v183
	v_mov_b32_e32 v158, v183
	v_mov_b32_e32 v159, v183
	v_mov_b32_e32 v160, v183
	v_mov_b32_e32 v161, v183
	v_mov_b32_e32 v162, v183
	v_mov_b32_e32 v163, v183
	v_mov_b32_e32 v164, v183
	v_mov_b32_e32 v165, v183
	v_mov_b32_e32 v166, v183
	v_mov_b32_e32 v167, v183
	v_mov_b32_e32 v168, v183
	v_mov_b32_e32 v169, v183
	v_mov_b32_e32 v170, v183
	v_mov_b32_e32 v171, v183
	v_mov_b32_e32 v172, v183
	v_mov_b32_e32 v173, v183
	v_mov_b32_e32 v174, v183
	v_mov_b32_e32 v175, v183
	v_mov_b32_e32 v176, v183
	v_mov_b32_e32 v177, v183
	s_and_b32 s0, s29, 0x10000
	v_add_u32_e32 v211, s0, v209
	v_add_u32_e32 v242, s0, v210
	s_barrier
